# speedup vs baseline: 1.0011x; 1.0011x over previous
.LBB2_4:
	s_or_b64 exec, exec, s[4:5]
	s_load_dwordx2 s[18:19], s[0:1], 0x48
	s_load_dwordx4 s[8:11], s[0:1], 0x38
	s_load_dwordx4 s[4:7], s[0:1], 0x10
	s_load_dwordx2 s[16:17], s[0:1], 0x20
	v_mov_b32_e32 v1, 0
	s_mov_b64 s[0:1], 0
	s_movk_i32 s24, 0x4b0
	s_waitcnt lgkmcnt(0)
	v_lshrrev_b32_e32 v118, 7, v0
	v_and_b32_e32 v119, 0x7f, v0
	s_mul_i32 s25, s22, 0x2ee
	s_mov_b64 s[20:21], 0x1000
	v_mul_u32_u24_e32 v120, 38, v118
	v_add_lshl_u32 v120, s25, v120, 9
	v_mov_b32_e32 v121, 0
	v_lshl_add_u64 v[122:123], s[16:17], 0, v[120:121]
	v_lshlrev_b32_e32 v120, 2, v119
	v_lshl_add_u64 v[122:123], v[122:123], 0, v[120:121]
	global_load_dword v80, v[122:123], off
	global_load_dword v81, v[122:123], off offset:512
	global_load_dword v82, v[122:123], off offset:1024
	global_load_dword v83, v[122:123], off offset:1536
	global_load_dword v84, v[122:123], off offset:2048
	global_load_dword v85, v[122:123], off offset:2560
	global_load_dword v86, v[122:123], off offset:3072
	global_load_dword v87, v[122:123], off offset:3584
	v_lshl_add_u64 v[122:123], v[122:123], 0, s[20:21]
	global_load_dword v88, v[122:123], off
	global_load_dword v89, v[122:123], off offset:512
	global_load_dword v90, v[122:123], off offset:1024
	global_load_dword v91, v[122:123], off offset:1536
	global_load_dword v92, v[122:123], off offset:2048
	global_load_dword v93, v[122:123], off offset:2560
	global_load_dword v94, v[122:123], off offset:3072
	global_load_dword v95, v[122:123], off offset:3584
	v_lshl_add_u64 v[122:123], v[122:123], 0, s[20:21]
	global_load_dword v96, v[122:123], off
	global_load_dword v97, v[122:123], off offset:512
	global_load_dword v98, v[122:123], off offset:1024
	global_load_dword v99, v[122:123], off offset:1536
	global_load_dword v100, v[122:123], off offset:2048
	global_load_dword v101, v[122:123], off offset:2560
	global_load_dword v102, v[122:123], off offset:3072
	global_load_dword v103, v[122:123], off offset:3584
	v_lshl_add_u64 v[122:123], v[122:123], 0, s[20:21]
	global_load_dword v104, v[122:123], off
	global_load_dword v105, v[122:123], off offset:512
	global_load_dword v106, v[122:123], off offset:1024
	global_load_dword v107, v[122:123], off offset:1536
	global_load_dword v108, v[122:123], off offset:2048
	global_load_dword v109, v[122:123], off offset:2560
	global_load_dword v110, v[122:123], off offset:3072
	global_load_dword v111, v[122:123], off offset:3584
	v_lshl_add_u64 v[122:123], v[122:123], 0, s[20:21]
	global_load_dword v112, v[122:123], off
	global_load_dword v113, v[122:123], off offset:512
	global_load_dword v114, v[122:123], off offset:1024
	global_load_dword v115, v[122:123], off offset:1536
	global_load_dword v116, v[122:123], off offset:2048
	global_load_dword v117, v[122:123], off offset:2560
	v_mov_b64_e32 v[2:3], s[14:15]
	s_movk_i32 s25, 0x4c0
	s_mov_b64 s[20:21], 0x400
	s_movk_i32 s26, 0xaf
	v_mov_b64_e32 v[4:5], v[0:1]

.LBB2_18:
	s_or_b64 exec, exec, s[0:1]
	v_lshrrev_b32_e32 v1, 7, v0
	v_and_b32_e32 v2, 0x7f, v0
	v_lshlrev_b32_e32 v38, 2, v2
	s_mul_i32 s8, s22, 0x2ee
	s_mov_b64 s[0:1], 0x1000
	v_mov_b32_e32 v5, 0
	v_mov_b32_e32 v6, v38
	v_mov_b32_e32 v7, 0
	v_mul_u32_u24_e32 v3, 19, v1
	v_add_lshl_u32 v4, s8, v3, 9
	v_lshl_add_u64 v[42:43], s[4:5], 0, v[4:5]
	v_lshl_add_u64 v[42:43], v[42:43], 0, v[6:7]
	v_lshl_add_u64 v[44:45], s[6:7], 0, v[4:5]
	v_lshl_add_u64 v[44:45], v[44:45], 0, v[6:7]
	v_mul_u32_u24_e32 v39, 0x98, v1
	v_add_u32_e32 v39, 0xe800, v39
	v_add_u32_e32 v71, 0x980, v39
	global_load_dword v2, v[42:43], off
	global_load_dword v3, v[44:45], off
	global_load_dword v4, v[42:43], off offset:512
	global_load_dword v5, v[44:45], off offset:512
	global_load_dword v6, v[42:43], off offset:1024
	global_load_dword v7, v[44:45], off offset:1024
	global_load_dword v8, v[42:43], off offset:1536
	global_load_dword v9, v[44:45], off offset:1536
	global_load_dword v10, v[42:43], off offset:2048
	global_load_dword v11, v[44:45], off offset:2048
	global_load_dword v12, v[42:43], off offset:2560
	global_load_dword v13, v[44:45], off offset:2560
	global_load_dword v14, v[42:43], off offset:3072
	global_load_dword v15, v[44:45], off offset:3072
	global_load_dword v16, v[42:43], off offset:3584
	global_load_dword v17, v[44:45], off offset:3584
	v_lshl_add_u64 v[42:43], v[42:43], 0, s[0:1]
	v_lshl_add_u64 v[44:45], v[44:45], 0, s[0:1]
	global_load_dword v18, v[42:43], off
	global_load_dword v19, v[44:45], off
	global_load_dword v20, v[42:43], off offset:512
	global_load_dword v21, v[44:45], off offset:512
	global_load_dword v22, v[42:43], off offset:1024
	global_load_dword v23, v[44:45], off offset:1024
	global_load_dword v24, v[42:43], off offset:1536
	global_load_dword v25, v[44:45], off offset:1536
	global_load_dword v26, v[42:43], off offset:2048
	global_load_dword v27, v[44:45], off offset:2048
	global_load_dword v28, v[42:43], off offset:2560
	global_load_dword v29, v[44:45], off offset:2560
	global_load_dword v30, v[42:43], off offset:3072
	global_load_dword v31, v[44:45], off offset:3072
	global_load_dword v32, v[42:43], off offset:3584
	global_load_dword v33, v[44:45], off offset:3584
	v_lshl_add_u64 v[42:43], v[42:43], 0, s[0:1]
	v_lshl_add_u64 v[44:45], v[44:45], 0, s[0:1]
	global_load_dword v34, v[42:43], off
	global_load_dword v35, v[44:45], off
	global_load_dword v36, v[42:43], off offset:512
	global_load_dword v37, v[44:45], off offset:512
	global_load_dword v118, v[42:43], off offset:1024
	global_load_dword v119, v[44:45], off offset:1024
	v_mov_b32_e32 v76, 0
	v_mov_b32_e32 v77, 0
	v_mov_b32_e32 v78, 0
	v_mov_b32_e32 v79, 0
	v_mov_b32_e32 v120, 0
	v_mov_b32_e32 v121, 0
	v_mov_b32_e32 v122, 0
	v_mov_b32_e32 v123, 0
	s_waitcnt lgkmcnt(0)
	s_barrier
	ds_read2_b64 v[40:43], v39 offset0:0 offset1:1
	ds_read2_b64 v[44:47], v39 offset0:152 offset1:153
	ds_read2_b64 v[48:51], v71 offset0:0 offset1:1
	ds_read2_b64 v[52:55], v71 offset0:152 offset1:153
	ds_read2_b64 v[56:59], v39 offset0:2 offset1:3
	ds_read2_b64 v[60:63], v39 offset0:154 offset1:155
	ds_read2_b64 v[64:67], v71 offset0:2 offset1:3
	ds_read2_b64 v[72:75], v71 offset0:154 offset1:155
	s_waitcnt vmcnt(38) lgkmcnt(4)
	v_pk_fma_f32 v[76:77], v[40:41], v[80:81], v[76:77]
	v_pk_fma_f32 v[78:79], v[44:45], v[80:81], v[78:79]
	v_pk_fma_f32 v[120:121], v[48:49], v[80:81], v[120:121]
	v_pk_fma_f32 v[122:123], v[52:53], v[80:81], v[122:123]
	v_pk_fma_f32 v[76:77], v[42:43], v[82:83], v[76:77]
	v_pk_fma_f32 v[78:79], v[46:47], v[82:83], v[78:79]
	v_pk_fma_f32 v[120:121], v[50:51], v[82:83], v[120:121]
	v_pk_fma_f32 v[122:123], v[54:55], v[82:83], v[122:123]
	ds_read2_b64 v[40:43], v39 offset0:4 offset1:5
	ds_read2_b64 v[44:47], v39 offset0:156 offset1:157
	ds_read2_b64 v[48:51], v71 offset0:4 offset1:5
	ds_read2_b64 v[52:55], v71 offset0:156 offset1:157
	s_waitcnt vmcnt(38) lgkmcnt(4)
	v_pk_fma_f32 v[76:77], v[56:57], v[84:85], v[76:77]
	v_pk_fma_f32 v[78:79], v[60:61], v[84:85], v[78:79]
	v_pk_fma_f32 v[120:121], v[64:65], v[84:85], v[120:121]
	v_pk_fma_f32 v[122:123], v[72:73], v[84:85], v[122:123]
	v_pk_fma_f32 v[76:77], v[58:59], v[86:87], v[76:77]
	v_pk_fma_f32 v[78:79], v[62:63], v[86:87], v[78:79]
	v_pk_fma_f32 v[120:121], v[66:67], v[86:87], v[120:121]
	v_pk_fma_f32 v[122:123], v[74:75], v[86:87], v[122:123]
	ds_read2_b64 v[56:59], v39 offset0:6 offset1:7
	ds_read2_b64 v[60:63], v39 offset0:158 offset1:159
	ds_read2_b64 v[64:67], v71 offset0:6 offset1:7
	ds_read2_b64 v[72:75], v71 offset0:158 offset1:159
	s_waitcnt vmcnt(38) lgkmcnt(4)
	v_pk_fma_f32 v[76:77], v[40:41], v[88:89], v[76:77]
	v_pk_fma_f32 v[78:79], v[44:45], v[88:89], v[78:79]
	v_pk_fma_f32 v[120:121], v[48:49], v[88:89], v[120:121]
	v_pk_fma_f32 v[122:123], v[52:53], v[88:89], v[122:123]
	v_pk_fma_f32 v[76:77], v[42:43], v[90:91], v[76:77]
	v_pk_fma_f32 v[78:79], v[46:47], v[90:91], v[78:79]
	v_pk_fma_f32 v[120:121], v[50:51], v[90:91], v[120:121]
	v_pk_fma_f32 v[122:123], v[54:55], v[90:91], v[122:123]
	ds_read2_b64 v[40:43], v39 offset0:8 offset1:9
	ds_read2_b64 v[44:47], v39 offset0:160 offset1:161
	ds_read2_b64 v[48:51], v71 offset0:8 offset1:9
	ds_read2_b64 v[52:55], v71 offset0:160 offset1:161
	s_waitcnt vmcnt(38) lgkmcnt(4)
	v_pk_fma_f32 v[76:77], v[56:57], v[92:93], v[76:77]
	v_pk_fma_f32 v[78:79], v[60:61], v[92:93], v[78:79]
	v_pk_fma_f32 v[120:121], v[64:65], v[92:93], v[120:121]
	v_pk_fma_f32 v[122:123], v[72:73], v[92:93], v[122:123]
	v_pk_fma_f32 v[76:77], v[58:59], v[94:95], v[76:77]
	v_pk_fma_f32 v[78:79], v[62:63], v[94:95], v[78:79]
	v_pk_fma_f32 v[120:121], v[66:67], v[94:95], v[120:121]
	v_pk_fma_f32 v[122:123], v[74:75], v[94:95], v[122:123]
	ds_read2_b64 v[56:59], v39 offset0:10 offset1:11
	ds_read2_b64 v[60:63], v39 offset0:162 offset1:163
	ds_read2_b64 v[64:67], v71 offset0:10 offset1:11
	ds_read2_b64 v[72:75], v71 offset0:162 offset1:163
	s_waitcnt vmcnt(38) lgkmcnt(4)
	v_pk_fma_f32 v[76:77], v[40:41], v[96:97], v[76:77]
	v_pk_fma_f32 v[78:79], v[44:45], v[96:97], v[78:79]
	v_pk_fma_f32 v[120:121], v[48:49], v[96:97], v[120:121]
	v_pk_fma_f32 v[122:123], v[52:53], v[96:97], v[122:123]
	v_pk_fma_f32 v[76:77], v[42:43], v[98:99], v[76:77]
	v_pk_fma_f32 v[78:79], v[46:47], v[98:99], v[78:79]
	v_pk_fma_f32 v[120:121], v[50:51], v[98:99], v[120:121]
	v_pk_fma_f32 v[122:123], v[54:55], v[98:99], v[122:123]
	ds_read2_b64 v[40:43], v39 offset0:12 offset1:13
	ds_read2_b64 v[44:47], v39 offset0:164 offset1:165
	ds_read2_b64 v[48:51], v71 offset0:12 offset1:13
	ds_read2_b64 v[52:55], v71 offset0:164 offset1:165
	s_waitcnt vmcnt(38) lgkmcnt(4)
	v_pk_fma_f32 v[76:77], v[56:57], v[100:101], v[76:77]
	v_pk_fma_f32 v[78:79], v[60:61], v[100:101], v[78:79]
	v_pk_fma_f32 v[120:121], v[64:65], v[100:101], v[120:121]
	v_pk_fma_f32 v[122:123], v[72:73], v[100:101], v[122:123]
	v_pk_fma_f32 v[76:77], v[58:59], v[102:103], v[76:77]
	v_pk_fma_f32 v[78:79], v[62:63], v[102:103], v[78:79]
	v_pk_fma_f32 v[120:121], v[66:67], v[102:103], v[120:121]
	v_pk_fma_f32 v[122:123], v[74:75], v[102:103], v[122:123]
	ds_read2_b64 v[56:59], v39 offset0:14 offset1:15
	ds_read2_b64 v[60:63], v39 offset0:166 offset1:167
	ds_read2_b64 v[64:67], v71 offset0:14 offset1:15
	ds_read2_b64 v[72:75], v71 offset0:166 offset1:167
	s_waitcnt vmcnt(38) lgkmcnt(4)
	v_pk_fma_f32 v[76:77], v[40:41], v[104:105], v[76:77]
	v_pk_fma_f32 v[78:79], v[44:45], v[104:105], v[78:79]
	v_pk_fma_f32 v[120:121], v[48:49], v[104:105], v[120:121]
	v_pk_fma_f32 v[122:123], v[52:53], v[104:105], v[122:123]
	v_pk_fma_f32 v[76:77], v[42:43], v[106:107], v[76:77]
	v_pk_fma_f32 v[78:79], v[46:47], v[106:107], v[78:79]
	v_pk_fma_f32 v[120:121], v[50:51], v[106:107], v[120:121]
	v_pk_fma_f32 v[122:123], v[54:55], v[106:107], v[122:123]
	ds_read2_b64 v[40:43], v39 offset0:16 offset1:17
	ds_read2_b64 v[44:47], v39 offset0:168 offset1:169
	ds_read2_b64 v[48:51], v71 offset0:16 offset1:17
	ds_read2_b64 v[52:55], v71 offset0:168 offset1:169
	s_waitcnt vmcnt(38) lgkmcnt(4)
	v_pk_fma_f32 v[76:77], v[56:57], v[108:109], v[76:77]
	v_pk_fma_f32 v[78:79], v[60:61], v[108:109], v[78:79]
	v_pk_fma_f32 v[120:121], v[64:65], v[108:109], v[120:121]
	v_pk_fma_f32 v[122:123], v[72:73], v[108:109], v[122:123]
	v_pk_fma_f32 v[76:77], v[58:59], v[110:111], v[76:77]
	v_pk_fma_f32 v[78:79], v[62:63], v[110:111], v[78:79]
	v_pk_fma_f32 v[120:121], v[66:67], v[110:111], v[120:121]
	v_pk_fma_f32 v[122:123], v[74:75], v[110:111], v[122:123]
	ds_read2_b64 v[56:59], v39 offset0:18 offset1:19
	ds_read2_b64 v[60:63], v39 offset0:170 offset1:171
	ds_read2_b64 v[64:67], v71 offset0:18 offset1:19
	ds_read2_b64 v[72:75], v71 offset0:170 offset1:171
	s_waitcnt vmcnt(38) lgkmcnt(4)
	v_pk_fma_f32 v[76:77], v[40:41], v[112:113], v[76:77]
	v_pk_fma_f32 v[78:79], v[44:45], v[112:113], v[78:79]
	v_pk_fma_f32 v[120:121], v[48:49], v[112:113], v[120:121]
	v_pk_fma_f32 v[122:123], v[52:53], v[112:113], v[122:123]
	v_pk_fma_f32 v[76:77], v[42:43], v[114:115], v[76:77]
	v_pk_fma_f32 v[78:79], v[46:47], v[114:115], v[78:79]
	v_pk_fma_f32 v[120:121], v[50:51], v[114:115], v[120:121]
	v_pk_fma_f32 v[122:123], v[54:55], v[114:115], v[122:123]
	s_waitcnt vmcnt(38) lgkmcnt(0)
	v_pk_fma_f32 v[76:77], v[56:57], v[116:117], v[76:77]
	v_pk_fma_f32 v[78:79], v[60:61], v[116:117], v[78:79]
	v_pk_fma_f32 v[120:121], v[64:65], v[116:117], v[120:121]
	v_pk_fma_f32 v[122:123], v[72:73], v[116:117], v[122:123]
	v_mul_u32_u24_e32 v92, 0x4c, v1
	v_add_u32_e32 v92, 0xfb00, v92
	v_add_u32_e32 v93, 0x4c0, v92
	v_add_u32_e32 v94, 0x980, v92
	v_add_u32_e32 v95, 0xe40, v92
	v_add_u32_e32 v96, 0x1300, v92
	v_mov_b32_e32 v97, 0x427c0000
	s_mov_b32 s0, 0xc27c0000
	v_mov_b32_e32 v124, 1.0
	v_mov_b32_e32 v125, 1.0
	v_mov_b32_e32 v126, 0x4038aa3b
	v_mov_b32_e32 v127, 0x4038aa3b
	v_mov_b32_e32 v80, 0
	v_mov_b32_e32 v81, 0
	v_mov_b32_e32 v82, 0
	v_mov_b32_e32 v83, 0
	v_mov_b32_e32 v84, 0
	v_mov_b32_e32 v85, 0
	v_mov_b32_e32 v86, 0
	v_mov_b32_e32 v87, 0
	v_mov_b32_e32 v88, 0
	v_mov_b32_e32 v89, 0
	ds_read2_b32 v[40:41], v92 offset0:0 offset1:152
	ds_read2_b32 v[42:43], v93 offset0:0 offset1:152
	ds_read2_b32 v[44:45], v94 offset0:0 offset1:152
	ds_read2_b32 v[46:47], v95 offset0:0 offset1:152
	ds_read2_b32 v[48:49], v96 offset0:0 offset1:152
	s_waitcnt vmcnt(36)
	v_pk_mul_f32 v[90:91], v[2:3], v[126:127]
	s_nop 0
	v_med3_f32 v90, v90, s0, v97
	v_med3_f32 v91, v91, s0, v97
	v_exp_f32_e32 v68, v90
	v_exp_f32_e32 v69, v91
	s_waitcnt lgkmcnt(0)
	ds_read2_b32 v[50:51], v92 offset0:1 offset1:153
	ds_read2_b32 v[52:53], v93 offset0:1 offset1:153
	ds_read2_b32 v[54:55], v94 offset0:1 offset1:153
	ds_read2_b32 v[56:57], v95 offset0:1 offset1:153
	ds_read2_b32 v[58:59], v96 offset0:1 offset1:153
	v_pk_add_f32 v[88:89], v[88:89], v[48:49]
	v_pk_add_f32 v[74:75], v[48:49], v[48:49]
	v_pk_fma_f32 v[60:61], v[68:69], v[40:41], v[124:125] op_sel_hi:[0,1,1]
	v_pk_fma_f32 v[62:63], v[68:69], v[42:43], v[124:125] op_sel_hi:[0,1,1]
	v_pk_fma_f32 v[64:65], v[68:69], v[44:45], v[124:125] op_sel:[1,0,0]
	v_pk_fma_f32 v[66:67], v[68:69], v[46:47], v[124:125] op_sel:[1,0,0]
	v_rcp_f32_e32 v60, v60
	v_rcp_f32_e32 v61, v61
	v_rcp_f32_e32 v62, v62
	v_rcp_f32_e32 v63, v63
	v_rcp_f32_e32 v64, v64
	v_rcp_f32_e32 v65, v65
	v_rcp_f32_e32 v66, v66
	v_rcp_f32_e32 v67, v67
	s_waitcnt vmcnt(34)
	v_pk_mul_f32 v[90:91], v[4:5], v[126:127]
	s_nop 0
	v_med3_f32 v90, v90, s0, v97
	v_med3_f32 v91, v91, s0, v97
	v_exp_f32_e32 v72, v90
	v_exp_f32_e32 v73, v91
	v_pk_fma_f32 v[80:81], v[74:75], v[60:61], v[80:81] op_sel_hi:[0,1,1] neg_lo:[1,0,0] neg_hi:[1,0,0]
	v_pk_fma_f32 v[82:83], v[74:75], v[62:63], v[82:83] op_sel_hi:[0,1,1] neg_lo:[1,0,0] neg_hi:[1,0,0]
	v_pk_fma_f32 v[84:85], v[74:75], v[64:65], v[84:85] op_sel:[1,0,0] neg_lo:[1,0,0] neg_hi:[1,0,0]
	v_pk_fma_f32 v[86:87], v[74:75], v[66:67], v[86:87] op_sel:[1,0,0] neg_lo:[1,0,0] neg_hi:[1,0,0]
	s_waitcnt lgkmcnt(0)
	ds_read2_b32 v[40:41], v92 offset0:2 offset1:154
	ds_read2_b32 v[42:43], v93 offset0:2 offset1:154
	ds_read2_b32 v[44:45], v94 offset0:2 offset1:154
	ds_read2_b32 v[46:47], v95 offset0:2 offset1:154
	ds_read2_b32 v[48:49], v96 offset0:2 offset1:154
	v_pk_add_f32 v[88:89], v[88:89], v[58:59]
	v_pk_add_f32 v[74:75], v[58:59], v[58:59]
	v_pk_fma_f32 v[60:61], v[72:73], v[50:51], v[124:125] op_sel_hi:[0,1,1]
	v_pk_fma_f32 v[62:63], v[72:73], v[52:53], v[124:125] op_sel_hi:[0,1,1]
	v_pk_fma_f32 v[64:65], v[72:73], v[54:55], v[124:125] op_sel:[1,0,0]
	v_pk_fma_f32 v[66:67], v[72:73], v[56:57], v[124:125] op_sel:[1,0,0]
	v_rcp_f32_e32 v60, v60
	v_rcp_f32_e32 v61, v61
	v_rcp_f32_e32 v62, v62
	v_rcp_f32_e32 v63, v63
	v_rcp_f32_e32 v64, v64
	v_rcp_f32_e32 v65, v65
	v_rcp_f32_e32 v66, v66
	v_rcp_f32_e32 v67, v67
	s_waitcnt vmcnt(32)
	v_pk_mul_f32 v[90:91], v[6:7], v[126:127]
	s_nop 0
	v_med3_f32 v90, v90, s0, v97
	v_med3_f32 v91, v91, s0, v97
	v_exp_f32_e32 v68, v90
	v_exp_f32_e32 v69, v91
	v_pk_fma_f32 v[80:81], v[74:75], v[60:61], v[80:81] op_sel_hi:[0,1,1] neg_lo:[1,0,0] neg_hi:[1,0,0]
	v_pk_fma_f32 v[82:83], v[74:75], v[62:63], v[82:83] op_sel_hi:[0,1,1] neg_lo:[1,0,0] neg_hi:[1,0,0]
	v_pk_fma_f32 v[84:85], v[74:75], v[64:65], v[84:85] op_sel:[1,0,0] neg_lo:[1,0,0] neg_hi:[1,0,0]
	v_pk_fma_f32 v[86:87], v[74:75], v[66:67], v[86:87] op_sel:[1,0,0] neg_lo:[1,0,0] neg_hi:[1,0,0]
	s_waitcnt lgkmcnt(0)
	ds_read2_b32 v[50:51], v92 offset0:3 offset1:155
	ds_read2_b32 v[52:53], v93 offset0:3 offset1:155
	ds_read2_b32 v[54:55], v94 offset0:3 offset1:155
	ds_read2_b32 v[56:57], v95 offset0:3 offset1:155
	ds_read2_b32 v[58:59], v96 offset0:3 offset1:155
	v_pk_add_f32 v[88:89], v[88:89], v[48:49]
	v_pk_add_f32 v[74:75], v[48:49], v[48:49]
	v_pk_fma_f32 v[60:61], v[68:69], v[40:41], v[124:125] op_sel_hi:[0,1,1]
	v_pk_fma_f32 v[62:63], v[68:69], v[42:43], v[124:125] op_sel_hi:[0,1,1]
	v_pk_fma_f32 v[64:65], v[68:69], v[44:45], v[124:125] op_sel:[1,0,0]
	v_pk_fma_f32 v[66:67], v[68:69], v[46:47], v[124:125] op_sel:[1,0,0]
	v_rcp_f32_e32 v60, v60
	v_rcp_f32_e32 v61, v61
	v_rcp_f32_e32 v62, v62
	v_rcp_f32_e32 v63, v63
	v_rcp_f32_e32 v64, v64
	v_rcp_f32_e32 v65, v65
	v_rcp_f32_e32 v66, v66
	v_rcp_f32_e32 v67, v67
	s_waitcnt vmcnt(30)
	v_pk_mul_f32 v[90:91], v[8:9], v[126:127]
	s_nop 0
	v_med3_f32 v90, v90, s0, v97
	v_med3_f32 v91, v91, s0, v97
	v_exp_f32_e32 v72, v90
	v_exp_f32_e32 v73, v91
	v_pk_fma_f32 v[80:81], v[74:75], v[60:61], v[80:81] op_sel_hi:[0,1,1] neg_lo:[1,0,0] neg_hi:[1,0,0]
	v_pk_fma_f32 v[82:83], v[74:75], v[62:63], v[82:83] op_sel_hi:[0,1,1] neg_lo:[1,0,0] neg_hi:[1,0,0]
	v_pk_fma_f32 v[84:85], v[74:75], v[64:65], v[84:85] op_sel:[1,0,0] neg_lo:[1,0,0] neg_hi:[1,0,0]
	v_pk_fma_f32 v[86:87], v[74:75], v[66:67], v[86:87] op_sel:[1,0,0] neg_lo:[1,0,0] neg_hi:[1,0,0]
	s_waitcnt lgkmcnt(0)
	ds_read2_b32 v[40:41], v92 offset0:4 offset1:156
	ds_read2_b32 v[42:43], v93 offset0:4 offset1:156
	ds_read2_b32 v[44:45], v94 offset0:4 offset1:156
	ds_read2_b32 v[46:47], v95 offset0:4 offset1:156
	ds_read2_b32 v[48:49], v96 offset0:4 offset1:156
	v_pk_add_f32 v[88:89], v[88:89], v[58:59]
	v_pk_add_f32 v[74:75], v[58:59], v[58:59]
	v_pk_fma_f32 v[60:61], v[72:73], v[50:51], v[124:125] op_sel_hi:[0,1,1]
	v_pk_fma_f32 v[62:63], v[72:73], v[52:53], v[124:125] op_sel_hi:[0,1,1]
	v_pk_fma_f32 v[64:65], v[72:73], v[54:55], v[124:125] op_sel:[1,0,0]
	v_pk_fma_f32 v[66:67], v[72:73], v[56:57], v[124:125] op_sel:[1,0,0]
	v_rcp_f32_e32 v60, v60
	v_rcp_f32_e32 v61, v61
	v_rcp_f32_e32 v62, v62
	v_rcp_f32_e32 v63, v63
	v_rcp_f32_e32 v64, v64
	v_rcp_f32_e32 v65, v65
	v_rcp_f32_e32 v66, v66
	v_rcp_f32_e32 v67, v67
	s_waitcnt vmcnt(28)
	v_pk_mul_f32 v[90:91], v[10:11], v[126:127]
	s_nop 0
	v_med3_f32 v90, v90, s0, v97
	v_med3_f32 v91, v91, s0, v97
	v_exp_f32_e32 v68, v90
	v_exp_f32_e32 v69, v91
	v_pk_fma_f32 v[80:81], v[74:75], v[60:61], v[80:81] op_sel_hi:[0,1,1] neg_lo:[1,0,0] neg_hi:[1,0,0]
	v_pk_fma_f32 v[82:83], v[74:75], v[62:63], v[82:83] op_sel_hi:[0,1,1] neg_lo:[1,0,0] neg_hi:[1,0,0]
	v_pk_fma_f32 v[84:85], v[74:75], v[64:65], v[84:85] op_sel:[1,0,0] neg_lo:[1,0,0] neg_hi:[1,0,0]
	v_pk_fma_f32 v[86:87], v[74:75], v[66:67], v[86:87] op_sel:[1,0,0] neg_lo:[1,0,0] neg_hi:[1,0,0]
	s_waitcnt lgkmcnt(0)
	ds_read2_b32 v[50:51], v92 offset0:5 offset1:157
	ds_read2_b32 v[52:53], v93 offset0:5 offset1:157
	ds_read2_b32 v[54:55], v94 offset0:5 offset1:157
	ds_read2_b32 v[56:57], v95 offset0:5 offset1:157
	ds_read2_b32 v[58:59], v96 offset0:5 offset1:157
	v_pk_add_f32 v[88:89], v[88:89], v[48:49]
	v_pk_add_f32 v[74:75], v[48:49], v[48:49]
	v_pk_fma_f32 v[60:61], v[68:69], v[40:41], v[124:125] op_sel_hi:[0,1,1]
	v_pk_fma_f32 v[62:63], v[68:69], v[42:43], v[124:125] op_sel_hi:[0,1,1]
	v_pk_fma_f32 v[64:65], v[68:69], v[44:45], v[124:125] op_sel:[1,0,0]
	v_pk_fma_f32 v[66:67], v[68:69], v[46:47], v[124:125] op_sel:[1,0,0]
	v_rcp_f32_e32 v60, v60
	v_rcp_f32_e32 v61, v61
	v_rcp_f32_e32 v62, v62
	v_rcp_f32_e32 v63, v63
	v_rcp_f32_e32 v64, v64
	v_rcp_f32_e32 v65, v65
	v_rcp_f32_e32 v66, v66
	v_rcp_f32_e32 v67, v67
	s_waitcnt vmcnt(26)
	v_pk_mul_f32 v[90:91], v[12:13], v[126:127]
	s_nop 0
	v_med3_f32 v90, v90, s0, v97
	v_med3_f32 v91, v91, s0, v97
	v_exp_f32_e32 v72, v90
	v_exp_f32_e32 v73, v91
	v_pk_fma_f32 v[80:81], v[74:75], v[60:61], v[80:81] op_sel_hi:[0,1,1] neg_lo:[1,0,0] neg_hi:[1,0,0]
	v_pk_fma_f32 v[82:83], v[74:75], v[62:63], v[82:83] op_sel_hi:[0,1,1] neg_lo:[1,0,0] neg_hi:[1,0,0]
	v_pk_fma_f32 v[84:85], v[74:75], v[64:65], v[84:85] op_sel:[1,0,0] neg_lo:[1,0,0] neg_hi:[1,0,0]
	v_pk_fma_f32 v[86:87], v[74:75], v[66:67], v[86:87] op_sel:[1,0,0] neg_lo:[1,0,0] neg_hi:[1,0,0]
	s_waitcnt lgkmcnt(0)
	ds_read2_b32 v[40:41], v92 offset0:6 offset1:158
	ds_read2_b32 v[42:43], v93 offset0:6 offset1:158
	ds_read2_b32 v[44:45], v94 offset0:6 offset1:158
	ds_read2_b32 v[46:47], v95 offset0:6 offset1:158
	ds_read2_b32 v[48:49], v96 offset0:6 offset1:158
	v_pk_add_f32 v[88:89], v[88:89], v[58:59]
	v_pk_add_f32 v[74:75], v[58:59], v[58:59]
	v_pk_fma_f32 v[60:61], v[72:73], v[50:51], v[124:125] op_sel_hi:[0,1,1]
	v_pk_fma_f32 v[62:63], v[72:73], v[52:53], v[124:125] op_sel_hi:[0,1,1]
	v_pk_fma_f32 v[64:65], v[72:73], v[54:55], v[124:125] op_sel:[1,0,0]
	v_pk_fma_f32 v[66:67], v[72:73], v[56:57], v[124:125] op_sel:[1,0,0]
	v_rcp_f32_e32 v60, v60
	v_rcp_f32_e32 v61, v61
	v_rcp_f32_e32 v62, v62
	v_rcp_f32_e32 v63, v63
	v_rcp_f32_e32 v64, v64
	v_rcp_f32_e32 v65, v65
	v_rcp_f32_e32 v66, v66
	v_rcp_f32_e32 v67, v67
	s_waitcnt vmcnt(24)
	v_pk_mul_f32 v[90:91], v[14:15], v[126:127]
	s_nop 0
	v_med3_f32 v90, v90, s0, v97
	v_med3_f32 v91, v91, s0, v97
	v_exp_f32_e32 v68, v90
	v_exp_f32_e32 v69, v91
	v_pk_fma_f32 v[80:81], v[74:75], v[60:61], v[80:81] op_sel_hi:[0,1,1] neg_lo:[1,0,0] neg_hi:[1,0,0]
	v_pk_fma_f32 v[82:83], v[74:75], v[62:63], v[82:83] op_sel_hi:[0,1,1] neg_lo:[1,0,0] neg_hi:[1,0,0]
	v_pk_fma_f32 v[84:85], v[74:75], v[64:65], v[84:85] op_sel:[1,0,0] neg_lo:[1,0,0] neg_hi:[1,0,0]
	v_pk_fma_f32 v[86:87], v[74:75], v[66:67], v[86:87] op_sel:[1,0,0] neg_lo:[1,0,0] neg_hi:[1,0,0]
	s_waitcnt lgkmcnt(0)
	ds_read2_b32 v[50:51], v92 offset0:7 offset1:159
	ds_read2_b32 v[52:53], v93 offset0:7 offset1:159
	ds_read2_b32 v[54:55], v94 offset0:7 offset1:159
	ds_read2_b32 v[56:57], v95 offset0:7 offset1:159
	ds_read2_b32 v[58:59], v96 offset0:7 offset1:159
	v_pk_add_f32 v[88:89], v[88:89], v[48:49]
	v_pk_add_f32 v[74:75], v[48:49], v[48:49]
	v_pk_fma_f32 v[60:61], v[68:69], v[40:41], v[124:125] op_sel_hi:[0,1,1]
	v_pk_fma_f32 v[62:63], v[68:69], v[42:43], v[124:125] op_sel_hi:[0,1,1]
	v_pk_fma_f32 v[64:65], v[68:69], v[44:45], v[124:125] op_sel:[1,0,0]
	v_pk_fma_f32 v[66:67], v[68:69], v[46:47], v[124:125] op_sel:[1,0,0]
	v_rcp_f32_e32 v60, v60
	v_rcp_f32_e32 v61, v61
	v_rcp_f32_e32 v62, v62
	v_rcp_f32_e32 v63, v63
	v_rcp_f32_e32 v64, v64
	v_rcp_f32_e32 v65, v65
	v_rcp_f32_e32 v66, v66
	v_rcp_f32_e32 v67, v67
	s_waitcnt vmcnt(22)
	v_pk_mul_f32 v[90:91], v[16:17], v[126:127]
	s_nop 0
	v_med3_f32 v90, v90, s0, v97
	v_med3_f32 v91, v91, s0, v97
	v_exp_f32_e32 v72, v90
	v_exp_f32_e32 v73, v91
	v_pk_fma_f32 v[80:81], v[74:75], v[60:61], v[80:81] op_sel_hi:[0,1,1] neg_lo:[1,0,0] neg_hi:[1,0,0]
	v_pk_fma_f32 v[82:83], v[74:75], v[62:63], v[82:83] op_sel_hi:[0,1,1] neg_lo:[1,0,0] neg_hi:[1,0,0]
	v_pk_fma_f32 v[84:85], v[74:75], v[64:65], v[84:85] op_sel:[1,0,0] neg_lo:[1,0,0] neg_hi:[1,0,0]
	v_pk_fma_f32 v[86:87], v[74:75], v[66:67], v[86:87] op_sel:[1,0,0] neg_lo:[1,0,0] neg_hi:[1,0,0]
	s_waitcnt lgkmcnt(0)
	ds_read2_b32 v[40:41], v92 offset0:8 offset1:160
	ds_read2_b32 v[42:43], v93 offset0:8 offset1:160
	ds_read2_b32 v[44:45], v94 offset0:8 offset1:160
	ds_read2_b32 v[46:47], v95 offset0:8 offset1:160
	ds_read2_b32 v[48:49], v96 offset0:8 offset1:160
	v_pk_add_f32 v[88:89], v[88:89], v[58:59]
	v_pk_add_f32 v[74:75], v[58:59], v[58:59]
	v_pk_fma_f32 v[60:61], v[72:73], v[50:51], v[124:125] op_sel_hi:[0,1,1]
	v_pk_fma_f32 v[62:63], v[72:73], v[52:53], v[124:125] op_sel_hi:[0,1,1]
	v_pk_fma_f32 v[64:65], v[72:73], v[54:55], v[124:125] op_sel:[1,0,0]
	v_pk_fma_f32 v[66:67], v[72:73], v[56:57], v[124:125] op_sel:[1,0,0]
	v_rcp_f32_e32 v60, v60
	v_rcp_f32_e32 v61, v61
	v_rcp_f32_e32 v62, v62
	v_rcp_f32_e32 v63, v63
	v_rcp_f32_e32 v64, v64
	v_rcp_f32_e32 v65, v65
	v_rcp_f32_e32 v66, v66
	v_rcp_f32_e32 v67, v67
	s_waitcnt vmcnt(20)
	v_pk_mul_f32 v[90:91], v[18:19], v[126:127]
	s_nop 0
	v_med3_f32 v90, v90, s0, v97
	v_med3_f32 v91, v91, s0, v97
	v_exp_f32_e32 v68, v90
	v_exp_f32_e32 v69, v91
	v_pk_fma_f32 v[80:81], v[74:75], v[60:61], v[80:81] op_sel_hi:[0,1,1] neg_lo:[1,0,0] neg_hi:[1,0,0]
	v_pk_fma_f32 v[82:83], v[74:75], v[62:63], v[82:83] op_sel_hi:[0,1,1] neg_lo:[1,0,0] neg_hi:[1,0,0]
	v_pk_fma_f32 v[84:85], v[74:75], v[64:65], v[84:85] op_sel:[1,0,0] neg_lo:[1,0,0] neg_hi:[1,0,0]
	v_pk_fma_f32 v[86:87], v[74:75], v[66:67], v[86:87] op_sel:[1,0,0] neg_lo:[1,0,0] neg_hi:[1,0,0]
	s_waitcnt lgkmcnt(0)
	ds_read2_b32 v[50:51], v92 offset0:9 offset1:161
	ds_read2_b32 v[52:53], v93 offset0:9 offset1:161
	ds_read2_b32 v[54:55], v94 offset0:9 offset1:161
	ds_read2_b32 v[56:57], v95 offset0:9 offset1:161
	ds_read2_b32 v[58:59], v96 offset0:9 offset1:161
	v_pk_add_f32 v[88:89], v[88:89], v[48:49]
	v_pk_add_f32 v[74:75], v[48:49], v[48:49]
	v_pk_fma_f32 v[60:61], v[68:69], v[40:41], v[124:125] op_sel_hi:[0,1,1]
	v_pk_fma_f32 v[62:63], v[68:69], v[42:43], v[124:125] op_sel_hi:[0,1,1]
	v_pk_fma_f32 v[64:65], v[68:69], v[44:45], v[124:125] op_sel:[1,0,0]
	v_pk_fma_f32 v[66:67], v[68:69], v[46:47], v[124:125] op_sel:[1,0,0]
	v_rcp_f32_e32 v60, v60
	v_rcp_f32_e32 v61, v61
	v_rcp_f32_e32 v62, v62
	v_rcp_f32_e32 v63, v63
	v_rcp_f32_e32 v64, v64
	v_rcp_f32_e32 v65, v65
	v_rcp_f32_e32 v66, v66
	v_rcp_f32_e32 v67, v67
	s_waitcnt vmcnt(18)
	v_pk_mul_f32 v[90:91], v[20:21], v[126:127]
	s_nop 0
	v_med3_f32 v90, v90, s0, v97
	v_med3_f32 v91, v91, s0, v97
	v_exp_f32_e32 v72, v90
	v_exp_f32_e32 v73, v91
	v_pk_fma_f32 v[80:81], v[74:75], v[60:61], v[80:81] op_sel_hi:[0,1,1] neg_lo:[1,0,0] neg_hi:[1,0,0]
	v_pk_fma_f32 v[82:83], v[74:75], v[62:63], v[82:83] op_sel_hi:[0,1,1] neg_lo:[1,0,0] neg_hi:[1,0,0]
	v_pk_fma_f32 v[84:85], v[74:75], v[64:65], v[84:85] op_sel:[1,0,0] neg_lo:[1,0,0] neg_hi:[1,0,0]
	v_pk_fma_f32 v[86:87], v[74:75], v[66:67], v[86:87] op_sel:[1,0,0] neg_lo:[1,0,0] neg_hi:[1,0,0]
	s_waitcnt lgkmcnt(0)
	ds_read2_b32 v[40:41], v92 offset0:10 offset1:162
	ds_read2_b32 v[42:43], v93 offset0:10 offset1:162
	ds_read2_b32 v[44:45], v94 offset0:10 offset1:162
	ds_read2_b32 v[46:47], v95 offset0:10 offset1:162
	ds_read2_b32 v[48:49], v96 offset0:10 offset1:162
	v_pk_add_f32 v[88:89], v[88:89], v[58:59]
	v_pk_add_f32 v[74:75], v[58:59], v[58:59]
	v_pk_fma_f32 v[60:61], v[72:73], v[50:51], v[124:125] op_sel_hi:[0,1,1]
	v_pk_fma_f32 v[62:63], v[72:73], v[52:53], v[124:125] op_sel_hi:[0,1,1]
	v_pk_fma_f32 v[64:65], v[72:73], v[54:55], v[124:125] op_sel:[1,0,0]
	v_pk_fma_f32 v[66:67], v[72:73], v[56:57], v[124:125] op_sel:[1,0,0]
	v_rcp_f32_e32 v60, v60
	v_rcp_f32_e32 v61, v61
	v_rcp_f32_e32 v62, v62
	v_rcp_f32_e32 v63, v63
	v_rcp_f32_e32 v64, v64
	v_rcp_f32_e32 v65, v65
	v_rcp_f32_e32 v66, v66
	v_rcp_f32_e32 v67, v67
	s_waitcnt vmcnt(16)
	v_pk_mul_f32 v[90:91], v[22:23], v[126:127]
	s_nop 0
	v_med3_f32 v90, v90, s0, v97
	v_med3_f32 v91, v91, s0, v97
	v_exp_f32_e32 v68, v90
	v_exp_f32_e32 v69, v91
	v_pk_fma_f32 v[80:81], v[74:75], v[60:61], v[80:81] op_sel_hi:[0,1,1] neg_lo:[1,0,0] neg_hi:[1,0,0]
	v_pk_fma_f32 v[82:83], v[74:75], v[62:63], v[82:83] op_sel_hi:[0,1,1] neg_lo:[1,0,0] neg_hi:[1,0,0]
	v_pk_fma_f32 v[84:85], v[74:75], v[64:65], v[84:85] op_sel:[1,0,0] neg_lo:[1,0,0] neg_hi:[1,0,0]
	v_pk_fma_f32 v[86:87], v[74:75], v[66:67], v[86:87] op_sel:[1,0,0] neg_lo:[1,0,0] neg_hi:[1,0,0]
	s_waitcnt lgkmcnt(0)
	ds_read2_b32 v[50:51], v92 offset0:11 offset1:163
	ds_read2_b32 v[52:53], v93 offset0:11 offset1:163
	ds_read2_b32 v[54:55], v94 offset0:11 offset1:163
	ds_read2_b32 v[56:57], v95 offset0:11 offset1:163
	ds_read2_b32 v[58:59], v96 offset0:11 offset1:163
	v_pk_add_f32 v[88:89], v[88:89], v[48:49]
	v_pk_add_f32 v[74:75], v[48:49], v[48:49]
	v_pk_fma_f32 v[60:61], v[68:69], v[40:41], v[124:125] op_sel_hi:[0,1,1]
	v_pk_fma_f32 v[62:63], v[68:69], v[42:43], v[124:125] op_sel_hi:[0,1,1]
	v_pk_fma_f32 v[64:65], v[68:69], v[44:45], v[124:125] op_sel:[1,0,0]
	v_pk_fma_f32 v[66:67], v[68:69], v[46:47], v[124:125] op_sel:[1,0,0]
	v_rcp_f32_e32 v60, v60
	v_rcp_f32_e32 v61, v61
	v_rcp_f32_e32 v62, v62
	v_rcp_f32_e32 v63, v63
	v_rcp_f32_e32 v64, v64
	v_rcp_f32_e32 v65, v65
	v_rcp_f32_e32 v66, v66
	v_rcp_f32_e32 v67, v67
	s_waitcnt vmcnt(14)
	v_pk_mul_f32 v[90:91], v[24:25], v[126:127]
	s_nop 0
	v_med3_f32 v90, v90, s0, v97
	v_med3_f32 v91, v91, s0, v97
	v_exp_f32_e32 v72, v90
	v_exp_f32_e32 v73, v91
	v_pk_fma_f32 v[80:81], v[74:75], v[60:61], v[80:81] op_sel_hi:[0,1,1] neg_lo:[1,0,0] neg_hi:[1,0,0]
	v_pk_fma_f32 v[82:83], v[74:75], v[62:63], v[82:83] op_sel_hi:[0,1,1] neg_lo:[1,0,0] neg_hi:[1,0,0]
	v_pk_fma_f32 v[84:85], v[74:75], v[64:65], v[84:85] op_sel:[1,0,0] neg_lo:[1,0,0] neg_hi:[1,0,0]
	v_pk_fma_f32 v[86:87], v[74:75], v[66:67], v[86:87] op_sel:[1,0,0] neg_lo:[1,0,0] neg_hi:[1,0,0]
	s_waitcnt lgkmcnt(0)
	ds_read2_b32 v[40:41], v92 offset0:12 offset1:164
	ds_read2_b32 v[42:43], v93 offset0:12 offset1:164
	ds_read2_b32 v[44:45], v94 offset0:12 offset1:164
	ds_read2_b32 v[46:47], v95 offset0:12 offset1:164
	ds_read2_b32 v[48:49], v96 offset0:12 offset1:164
	v_pk_add_f32 v[88:89], v[88:89], v[58:59]
	v_pk_add_f32 v[74:75], v[58:59], v[58:59]
	v_pk_fma_f32 v[60:61], v[72:73], v[50:51], v[124:125] op_sel_hi:[0,1,1]
	v_pk_fma_f32 v[62:63], v[72:73], v[52:53], v[124:125] op_sel_hi:[0,1,1]
	v_pk_fma_f32 v[64:65], v[72:73], v[54:55], v[124:125] op_sel:[1,0,0]
	v_pk_fma_f32 v[66:67], v[72:73], v[56:57], v[124:125] op_sel:[1,0,0]
	v_rcp_f32_e32 v60, v60
	v_rcp_f32_e32 v61, v61
	v_rcp_f32_e32 v62, v62
	v_rcp_f32_e32 v63, v63
	v_rcp_f32_e32 v64, v64
	v_rcp_f32_e32 v65, v65
	v_rcp_f32_e32 v66, v66
	v_rcp_f32_e32 v67, v67
	s_waitcnt vmcnt(12)
	v_pk_mul_f32 v[90:91], v[26:27], v[126:127]
	s_nop 0
	v_med3_f32 v90, v90, s0, v97
	v_med3_f32 v91, v91, s0, v97
	v_exp_f32_e32 v68, v90
	v_exp_f32_e32 v69, v91
	v_pk_fma_f32 v[80:81], v[74:75], v[60:61], v[80:81] op_sel_hi:[0,1,1] neg_lo:[1,0,0] neg_hi:[1,0,0]
	v_pk_fma_f32 v[82:83], v[74:75], v[62:63], v[82:83] op_sel_hi:[0,1,1] neg_lo:[1,0,0] neg_hi:[1,0,0]
	v_pk_fma_f32 v[84:85], v[74:75], v[64:65], v[84:85] op_sel:[1,0,0] neg_lo:[1,0,0] neg_hi:[1,0,0]
	v_pk_fma_f32 v[86:87], v[74:75], v[66:67], v[86:87] op_sel:[1,0,0] neg_lo:[1,0,0] neg_hi:[1,0,0]
	s_waitcnt lgkmcnt(0)
	ds_read2_b32 v[50:51], v92 offset0:13 offset1:165
	ds_read2_b32 v[52:53], v93 offset0:13 offset1:165
	ds_read2_b32 v[54:55], v94 offset0:13 offset1:165
	ds_read2_b32 v[56:57], v95 offset0:13 offset1:165
	ds_read2_b32 v[58:59], v96 offset0:13 offset1:165
	v_pk_add_f32 v[88:89], v[88:89], v[48:49]
	v_pk_add_f32 v[74:75], v[48:49], v[48:49]
	v_pk_fma_f32 v[60:61], v[68:69], v[40:41], v[124:125] op_sel_hi:[0,1,1]
	v_pk_fma_f32 v[62:63], v[68:69], v[42:43], v[124:125] op_sel_hi:[0,1,1]
	v_pk_fma_f32 v[64:65], v[68:69], v[44:45], v[124:125] op_sel:[1,0,0]
	v_pk_fma_f32 v[66:67], v[68:69], v[46:47], v[124:125] op_sel:[1,0,0]
	v_rcp_f32_e32 v60, v60
	v_rcp_f32_e32 v61, v61
	v_rcp_f32_e32 v62, v62
	v_rcp_f32_e32 v63, v63
	v_rcp_f32_e32 v64, v64
	v_rcp_f32_e32 v65, v65
	v_rcp_f32_e32 v66, v66
	v_rcp_f32_e32 v67, v67
	s_waitcnt vmcnt(10)
	v_pk_mul_f32 v[90:91], v[28:29], v[126:127]
	s_nop 0
	v_med3_f32 v90, v90, s0, v97
	v_med3_f32 v91, v91, s0, v97
	v_exp_f32_e32 v72, v90
	v_exp_f32_e32 v73, v91
	v_pk_fma_f32 v[80:81], v[74:75], v[60:61], v[80:81] op_sel_hi:[0,1,1] neg_lo:[1,0,0] neg_hi:[1,0,0]
	v_pk_fma_f32 v[82:83], v[74:75], v[62:63], v[82:83] op_sel_hi:[0,1,1] neg_lo:[1,0,0] neg_hi:[1,0,0]
	v_pk_fma_f32 v[84:85], v[74:75], v[64:65], v[84:85] op_sel:[1,0,0] neg_lo:[1,0,0] neg_hi:[1,0,0]
	v_pk_fma_f32 v[86:87], v[74:75], v[66:67], v[86:87] op_sel:[1,0,0] neg_lo:[1,0,0] neg_hi:[1,0,0]
	s_waitcnt lgkmcnt(0)
	ds_read2_b32 v[40:41], v92 offset0:14 offset1:166
	ds_read2_b32 v[42:43], v93 offset0:14 offset1:166
	ds_read2_b32 v[44:45], v94 offset0:14 offset1:166
	ds_read2_b32 v[46:47], v95 offset0:14 offset1:166
	ds_read2_b32 v[48:49], v96 offset0:14 offset1:166
	v_pk_add_f32 v[88:89], v[88:89], v[58:59]
	v_pk_add_f32 v[74:75], v[58:59], v[58:59]
	v_pk_fma_f32 v[60:61], v[72:73], v[50:51], v[124:125] op_sel_hi:[0,1,1]
	v_pk_fma_f32 v[62:63], v[72:73], v[52:53], v[124:125] op_sel_hi:[0,1,1]
	v_pk_fma_f32 v[64:65], v[72:73], v[54:55], v[124:125] op_sel:[1,0,0]
	v_pk_fma_f32 v[66:67], v[72:73], v[56:57], v[124:125] op_sel:[1,0,0]
	v_rcp_f32_e32 v60, v60
	v_rcp_f32_e32 v61, v61
	v_rcp_f32_e32 v62, v62
	v_rcp_f32_e32 v63, v63
	v_rcp_f32_e32 v64, v64
	v_rcp_f32_e32 v65, v65
	v_rcp_f32_e32 v66, v66
	v_rcp_f32_e32 v67, v67
	s_waitcnt vmcnt(8)
	v_pk_mul_f32 v[90:91], v[30:31], v[126:127]
	s_nop 0
	v_med3_f32 v90, v90, s0, v97
	v_med3_f32 v91, v91, s0, v97
	v_exp_f32_e32 v68, v90
	v_exp_f32_e32 v69, v91
	v_pk_fma_f32 v[80:81], v[74:75], v[60:61], v[80:81] op_sel_hi:[0,1,1] neg_lo:[1,0,0] neg_hi:[1,0,0]
	v_pk_fma_f32 v[82:83], v[74:75], v[62:63], v[82:83] op_sel_hi:[0,1,1] neg_lo:[1,0,0] neg_hi:[1,0,0]
	v_pk_fma_f32 v[84:85], v[74:75], v[64:65], v[84:85] op_sel:[1,0,0] neg_lo:[1,0,0] neg_hi:[1,0,0]
	v_pk_fma_f32 v[86:87], v[74:75], v[66:67], v[86:87] op_sel:[1,0,0] neg_lo:[1,0,0] neg_hi:[1,0,0]
	s_waitcnt lgkmcnt(0)
	ds_read2_b32 v[50:51], v92 offset0:15 offset1:167
	ds_read2_b32 v[52:53], v93 offset0:15 offset1:167
	ds_read2_b32 v[54:55], v94 offset0:15 offset1:167
	ds_read2_b32 v[56:57], v95 offset0:15 offset1:167
	ds_read2_b32 v[58:59], v96 offset0:15 offset1:167
	v_pk_add_f32 v[88:89], v[88:89], v[48:49]
	v_pk_add_f32 v[74:75], v[48:49], v[48:49]
	v_pk_fma_f32 v[60:61], v[68:69], v[40:41], v[124:125] op_sel_hi:[0,1,1]
	v_pk_fma_f32 v[62:63], v[68:69], v[42:43], v[124:125] op_sel_hi:[0,1,1]
	v_pk_fma_f32 v[64:65], v[68:69], v[44:45], v[124:125] op_sel:[1,0,0]
	v_pk_fma_f32 v[66:67], v[68:69], v[46:47], v[124:125] op_sel:[1,0,0]
	v_rcp_f32_e32 v60, v60
	v_rcp_f32_e32 v61, v61
	v_rcp_f32_e32 v62, v62
	v_rcp_f32_e32 v63, v63
	v_rcp_f32_e32 v64, v64
	v_rcp_f32_e32 v65, v65
	v_rcp_f32_e32 v66, v66
	v_rcp_f32_e32 v67, v67
	s_waitcnt vmcnt(6)
	v_pk_mul_f32 v[90:91], v[32:33], v[126:127]
	s_nop 0
	v_med3_f32 v90, v90, s0, v97
	v_med3_f32 v91, v91, s0, v97
	v_exp_f32_e32 v72, v90
	v_exp_f32_e32 v73, v91
	v_pk_fma_f32 v[80:81], v[74:75], v[60:61], v[80:81] op_sel_hi:[0,1,1] neg_lo:[1,0,0] neg_hi:[1,0,0]
	v_pk_fma_f32 v[82:83], v[74:75], v[62:63], v[82:83] op_sel_hi:[0,1,1] neg_lo:[1,0,0] neg_hi:[1,0,0]
	v_pk_fma_f32 v[84:85], v[74:75], v[64:65], v[84:85] op_sel:[1,0,0] neg_lo:[1,0,0] neg_hi:[1,0,0]
	v_pk_fma_f32 v[86:87], v[74:75], v[66:67], v[86:87] op_sel:[1,0,0] neg_lo:[1,0,0] neg_hi:[1,0,0]
	s_waitcnt lgkmcnt(0)
	ds_read2_b32 v[40:41], v92 offset0:16 offset1:168
	ds_read2_b32 v[42:43], v93 offset0:16 offset1:168
	ds_read2_b32 v[44:45], v94 offset0:16 offset1:168
	ds_read2_b32 v[46:47], v95 offset0:16 offset1:168
	ds_read2_b32 v[48:49], v96 offset0:16 offset1:168
	v_pk_add_f32 v[88:89], v[88:89], v[58:59]
	v_pk_add_f32 v[74:75], v[58:59], v[58:59]
	v_pk_fma_f32 v[60:61], v[72:73], v[50:51], v[124:125] op_sel_hi:[0,1,1]
	v_pk_fma_f32 v[62:63], v[72:73], v[52:53], v[124:125] op_sel_hi:[0,1,1]
	v_pk_fma_f32 v[64:65], v[72:73], v[54:55], v[124:125] op_sel:[1,0,0]
	v_pk_fma_f32 v[66:67], v[72:73], v[56:57], v[124:125] op_sel:[1,0,0]
	v_rcp_f32_e32 v60, v60
	v_rcp_f32_e32 v61, v61
	v_rcp_f32_e32 v62, v62
	v_rcp_f32_e32 v63, v63
	v_rcp_f32_e32 v64, v64
	v_rcp_f32_e32 v65, v65
	v_rcp_f32_e32 v66, v66
	v_rcp_f32_e32 v67, v67
	s_waitcnt vmcnt(4)
	v_pk_mul_f32 v[90:91], v[34:35], v[126:127]
	s_nop 0
	v_med3_f32 v90, v90, s0, v97
	v_med3_f32 v91, v91, s0, v97
	v_exp_f32_e32 v68, v90
	v_exp_f32_e32 v69, v91
	v_pk_fma_f32 v[80:81], v[74:75], v[60:61], v[80:81] op_sel_hi:[0,1,1] neg_lo:[1,0,0] neg_hi:[1,0,0]
	v_pk_fma_f32 v[82:83], v[74:75], v[62:63], v[82:83] op_sel_hi:[0,1,1] neg_lo:[1,0,0] neg_hi:[1,0,0]
	v_pk_fma_f32 v[84:85], v[74:75], v[64:65], v[84:85] op_sel:[1,0,0] neg_lo:[1,0,0] neg_hi:[1,0,0]
	v_pk_fma_f32 v[86:87], v[74:75], v[66:67], v[86:87] op_sel:[1,0,0] neg_lo:[1,0,0] neg_hi:[1,0,0]
	s_waitcnt lgkmcnt(0)
	ds_read2_b32 v[50:51], v92 offset0:17 offset1:169
	ds_read2_b32 v[52:53], v93 offset0:17 offset1:169
	ds_read2_b32 v[54:55], v94 offset0:17 offset1:169
	ds_read2_b32 v[56:57], v95 offset0:17 offset1:169
	ds_read2_b32 v[58:59], v96 offset0:17 offset1:169
	v_pk_add_f32 v[88:89], v[88:89], v[48:49]
	v_pk_add_f32 v[74:75], v[48:49], v[48:49]
	v_pk_fma_f32 v[60:61], v[68:69], v[40:41], v[124:125] op_sel_hi:[0,1,1]
	v_pk_fma_f32 v[62:63], v[68:69], v[42:43], v[124:125] op_sel_hi:[0,1,1]
	v_pk_fma_f32 v[64:65], v[68:69], v[44:45], v[124:125] op_sel:[1,0,0]
	v_pk_fma_f32 v[66:67], v[68:69], v[46:47], v[124:125] op_sel:[1,0,0]
	v_rcp_f32_e32 v60, v60
	v_rcp_f32_e32 v61, v61
	v_rcp_f32_e32 v62, v62
	v_rcp_f32_e32 v63, v63
	v_rcp_f32_e32 v64, v64
	v_rcp_f32_e32 v65, v65
	v_rcp_f32_e32 v66, v66
	v_rcp_f32_e32 v67, v67
	s_waitcnt vmcnt(2)
	v_pk_mul_f32 v[90:91], v[36:37], v[126:127]
	s_nop 0
	v_med3_f32 v90, v90, s0, v97
	v_med3_f32 v91, v91, s0, v97
	v_exp_f32_e32 v72, v90
	v_exp_f32_e32 v73, v91
	v_pk_fma_f32 v[80:81], v[74:75], v[60:61], v[80:81] op_sel_hi:[0,1,1] neg_lo:[1,0,0] neg_hi:[1,0,0]
	v_pk_fma_f32 v[82:83], v[74:75], v[62:63], v[82:83] op_sel_hi:[0,1,1] neg_lo:[1,0,0] neg_hi:[1,0,0]
	v_pk_fma_f32 v[84:85], v[74:75], v[64:65], v[84:85] op_sel:[1,0,0] neg_lo:[1,0,0] neg_hi:[1,0,0]
	v_pk_fma_f32 v[86:87], v[74:75], v[66:67], v[86:87] op_sel:[1,0,0] neg_lo:[1,0,0] neg_hi:[1,0,0]
	s_waitcnt lgkmcnt(0)
	ds_read2_b32 v[40:41], v92 offset0:18 offset1:170
	ds_read2_b32 v[42:43], v93 offset0:18 offset1:170
	ds_read2_b32 v[44:45], v94 offset0:18 offset1:170
	ds_read2_b32 v[46:47], v95 offset0:18 offset1:170
	ds_read2_b32 v[48:49], v96 offset0:18 offset1:170
	v_pk_add_f32 v[88:89], v[88:89], v[58:59]
	v_pk_add_f32 v[74:75], v[58:59], v[58:59]
	v_pk_fma_f32 v[60:61], v[72:73], v[50:51], v[124:125] op_sel_hi:[0,1,1]
	v_pk_fma_f32 v[62:63], v[72:73], v[52:53], v[124:125] op_sel_hi:[0,1,1]
	v_pk_fma_f32 v[64:65], v[72:73], v[54:55], v[124:125] op_sel:[1,0,0]
	v_pk_fma_f32 v[66:67], v[72:73], v[56:57], v[124:125] op_sel:[1,0,0]
	v_rcp_f32_e32 v60, v60
	v_rcp_f32_e32 v61, v61
	v_rcp_f32_e32 v62, v62
	v_rcp_f32_e32 v63, v63
	v_rcp_f32_e32 v64, v64
	v_rcp_f32_e32 v65, v65
	v_rcp_f32_e32 v66, v66
	v_rcp_f32_e32 v67, v67
	s_waitcnt vmcnt(0)
	v_pk_mul_f32 v[90:91], v[118:119], v[126:127]
	s_nop 0
	v_med3_f32 v90, v90, s0, v97
	v_med3_f32 v91, v91, s0, v97
	v_exp_f32_e32 v68, v90
	v_exp_f32_e32 v69, v91
	v_pk_fma_f32 v[80:81], v[74:75], v[60:61], v[80:81] op_sel_hi:[0,1,1] neg_lo:[1,0,0] neg_hi:[1,0,0]
	v_pk_fma_f32 v[82:83], v[74:75], v[62:63], v[82:83] op_sel_hi:[0,1,1] neg_lo:[1,0,0] neg_hi:[1,0,0]
	v_pk_fma_f32 v[84:85], v[74:75], v[64:65], v[84:85] op_sel:[1,0,0] neg_lo:[1,0,0] neg_hi:[1,0,0]
	v_pk_fma_f32 v[86:87], v[74:75], v[66:67], v[86:87] op_sel:[1,0,0] neg_lo:[1,0,0] neg_hi:[1,0,0]
	s_waitcnt lgkmcnt(0)
	v_pk_add_f32 v[88:89], v[88:89], v[48:49]
	v_pk_add_f32 v[74:75], v[48:49], v[48:49]
	v_pk_fma_f32 v[60:61], v[68:69], v[40:41], v[124:125] op_sel_hi:[0,1,1]
	v_pk_fma_f32 v[62:63], v[68:69], v[42:43], v[124:125] op_sel_hi:[0,1,1]
	v_pk_fma_f32 v[64:65], v[68:69], v[44:45], v[124:125] op_sel:[1,0,0]
	v_pk_fma_f32 v[66:67], v[68:69], v[46:47], v[124:125] op_sel:[1,0,0]
	v_rcp_f32_e32 v60, v60
	v_rcp_f32_e32 v61, v61
	v_rcp_f32_e32 v62, v62
	v_rcp_f32_e32 v63, v63
	v_rcp_f32_e32 v64, v64
	v_rcp_f32_e32 v65, v65
	v_rcp_f32_e32 v66, v66
	v_rcp_f32_e32 v67, v67
	s_nop 0
	v_pk_fma_f32 v[80:81], v[74:75], v[60:61], v[80:81] op_sel_hi:[0,1,1] neg_lo:[1,0,0] neg_hi:[1,0,0]
	v_pk_fma_f32 v[82:83], v[74:75], v[62:63], v[82:83] op_sel_hi:[0,1,1] neg_lo:[1,0,0] neg_hi:[1,0,0]
	v_pk_fma_f32 v[84:85], v[74:75], v[64:65], v[84:85] op_sel:[1,0,0] neg_lo:[1,0,0] neg_hi:[1,0,0]
	v_pk_fma_f32 v[86:87], v[74:75], v[66:67], v[86:87] op_sel:[1,0,0] neg_lo:[1,0,0] neg_hi:[1,0,0]
	v_add_f32_e32 v80, v88, v80
	v_add_f32_e32 v81, v88, v81
	v_add_f32_e32 v82, v88, v82
	v_add_f32_e32 v83, v88, v83
	v_add_f32_e32 v84, v89, v84
	v_add_f32_e32 v85, v89, v85
	v_add_f32_e32 v86, v89, v86
	v_add_f32_e32 v87, v89, v87
	v_add_f32_e32 v76, v76, v77
	v_add_f32_e32 v78, v78, v79
	v_add_f32_e32 v120, v120, v121
	v_add_f32_e32 v122, v122, v123
	v_mul_u32_u24_e32 v6, 0x1800, v1
	v_or_b32_e32 v6, v38, v6
	ds_write2st64_b32 v6, v80, v81 offset1:2
	ds_write2st64_b32 v6, v82, v83 offset0:4 offset1:6
	ds_write2st64_b32 v6, v76, v78 offset0:8 offset1:10
	ds_write2st64_b32 v6, v120, v122 offset0:12 offset1:14
	ds_write2st64_b32 v6, v84, v85 offset0:16 offset1:18
	ds_write2st64_b32 v6, v86, v87 offset0:20 offset1:22
	v_or_b32_e32 v10, 0xc000, v38
	v_lshl_or_b32 v11, v1, 9, v38
	v_add_u32_e32 v1, 4, v1
	v_mov_b32_e32 v12, v0
	s_mov_b64 s[4:5], 0
	s_movk_i32 s8, 0x1ff
	s_movk_i32 s9, 0x3ff
	s_waitcnt lgkmcnt(0)
	s_barrier
	s_branch .LBB2_21
